# P6 K-loop: w_down streamer scale+fp8-convert VALU moved into the wave's own MMA4 segment (between MFMAs), same as P2
# baseline (speedup 1.0000x reference)
.LBB0_926:
	v_mov_b32_e32 v40, v202
	v_mov_b32_e32 v41, v219
	v_mov_b32_e32 v42, v220
	v_mov_b32_e32 v43, v221
	s_add_i32 s4, s94, s33
	s_mov_b32 s64, s90
	s_add_i32 s90, s90, 1
	s_add_i32 s3, s4, 0x200
	s_add_i32 s5, s61, s33
	ds_read_b128 v[24:27], v217 offset:0
	ds_read_b128 v[28:31], v217 offset:0x400
	ds_read_b128 v[16:19], v217 offset:0x800
	ds_read_b128 v[20:23], v217 offset:0xc00
	ds_read_b128 v[46:49], v216 offset:0
	ds_read_b128 v[50:53], v216 offset:0x400
	ds_read_b128 v[54:57], v216 offset:0x800
	ds_read_b128 v[58:61], v216 offset:0xc00
	ds_read_b128 v[192:195], v216 offset:0x1000
	ds_read_b128 v[196:199], v216 offset:0x1400
	ds_read_b128 v[220:223], v216 offset:0x1800
	ds_read_b128 v[224:227], v216 offset:0x1c00
	ds_read_b128 v[8:11], v217 offset:0x4000
	ds_read_b128 v[12:15], v217 offset:0x4400
	ds_read_b128 v[0:3], v217 offset:0x4800
	ds_read_b128 v[4:7], v217 offset:0x4c00
	s_cmpk_eq_i32 s33, 0xe00
	s_cselect_b32 s65, s60, s3
	s_cselect_b32 s16, s95, s5
	s_add_i32 s3, s65, 0x80
	s_mov_b32 m0, s86
	s_add_i32 s5, s4, 0x80180
	buffer_load_dwordx4 v214, s[12:15], s5 offen lds
	s_add_i32 s4, s4, 0xc0180
	s_mov_b32 m0, s89
	s_add_i32 s17, s16, 0x80
	buffer_load_dwordx4 v214, s[12:15], s4 offen lds
	s_lshr_b32 s4, s90, 2
	s_mul_i32 s5, s4, s34
	s_add_i32 s36, s5, s2
	s_cmp_lt_i32 s4, s47
	s_cselect_b64 s[4:5], -1, 0
	s_and_b64 s[62:63], s[4:5], exec
	s_cselect_b32 s67, s36, 0
	s_ashr_i32 s62, s67, 7
	s_bfe_u32 s36, s90, 0x10001
	s_ashr_i32 s63, s62, 31
	s_or_b32 s78, s36, s87
	s_bfe_u32 s36, s67, 0x20005
	s_lshl_b64 vcc, s[62:63], 23
	s_add_u32 vcc_lo, s28, vcc_lo
	s_addc_u32 vcc_hi, s29, vcc_hi
	s_lshl_b32 s38, s36, 21
	s_add_u32 s38, vcc_lo, s38
	s_addc_u32 s39, vcc_hi, 0
	s_lshl_b32 s67, s67, 7
	s_and_b32 s67, s67, 0xf80
	s_lshl_b32 vcc_lo, s67, 2
	s_add_u32 vcc_lo, s38, vcc_lo
	v_and_or_b32 v202, s79, 2, v200
	s_addc_u32 vcc_hi, s39, 0
	v_lshl_or_b32 v44, s78, 5, v218
	v_lshlrev_b64 v[32:33], 14, v[202:203]
	v_lshl_add_u64 v[32:33], vcc, 0, v[32:33]
	v_lshlrev_b32_e32 v202, 2, v44
	v_lshl_add_u64 v[32:33], v[32:33], 0, v[202:203]
	s_movk_i32 s38, 0x4000
	v_add_co_u32_e32 v36, vcc, s38, v32
	s_nop 1
	v_addc_co_u32_e32 v37, vcc, 0, v33, vcc
	global_load_dwordx4 v[32:35], v[32:33], off nt
	s_nop 0
	global_load_dwordx4 v[36:39], v[36:37], off nt
	s_waitcnt vmcnt(10)
	s_waitcnt lgkmcnt(4)
	s_barrier
	s_setprio 1
	v_mfma_scale_f32_16x16x128_f8f6f4 v[188:191], v[24:31], v[46:53], v[188:191], v213, v213 op_sel_hi:[0,0,0]
	v_mfma_scale_f32_16x16x128_f8f6f4 v[184:187], v[16:23], v[46:53], v[184:187], v213, v213 op_sel_hi:[0,0,0]
	v_mfma_scale_f32_16x16x128_f8f6f4 v[180:183], v[24:31], v[54:61], v[180:183], v213, v213 op_sel_hi:[0,0,0]
	v_mfma_scale_f32_16x16x128_f8f6f4 v[176:179], v[16:23], v[54:61], v[176:179], v213, v213 op_sel_hi:[0,0,0]
	v_mfma_scale_f32_16x16x128_f8f6f4 v[172:175], v[24:31], v[192:199], v[172:175], v213, v213 op_sel_hi:[0,0,0]
	v_mfma_scale_f32_16x16x128_f8f6f4 v[168:171], v[16:23], v[192:199], v[168:171], v213, v213 op_sel_hi:[0,0,0]
	v_mfma_scale_f32_16x16x128_f8f6f4 v[164:167], v[24:31], v[220:227], v[164:167], v213, v213 op_sel_hi:[0,0,0]
	v_mfma_scale_f32_16x16x128_f8f6f4 v[160:163], v[16:23], v[220:227], v[160:163], v213, v213 op_sel_hi:[0,0,0]
	s_setprio 0
	s_setprio 1
	s_waitcnt lgkmcnt(2)
	v_mfma_scale_f32_16x16x128_f8f6f4 v[156:159], v[8:15], v[46:53], v[156:159], v213, v213 op_sel_hi:[0,0,0]
	s_waitcnt lgkmcnt(0)
	v_mfma_scale_f32_16x16x128_f8f6f4 v[152:155], v[0:7], v[46:53], v[152:155], v213, v213 op_sel_hi:[0,0,0]
	v_mfma_scale_f32_16x16x128_f8f6f4 v[148:151], v[8:15], v[54:61], v[148:151], v213, v213 op_sel_hi:[0,0,0]
	v_mfma_scale_f32_16x16x128_f8f6f4 v[144:147], v[0:7], v[54:61], v[144:147], v213, v213 op_sel_hi:[0,0,0]
	v_mfma_scale_f32_16x16x128_f8f6f4 v[140:143], v[8:15], v[192:199], v[140:143], v213, v213 op_sel_hi:[0,0,0]
	v_mfma_scale_f32_16x16x128_f8f6f4 v[136:139], v[0:7], v[192:199], v[136:139], v213, v213 op_sel_hi:[0,0,0]
	v_mfma_scale_f32_16x16x128_f8f6f4 v[132:135], v[8:15], v[220:227], v[132:135], v213, v213 op_sel_hi:[0,0,0]
	v_mfma_scale_f32_16x16x128_f8f6f4 v[128:131], v[0:7], v[220:227], v[128:131], v213, v213 op_sel_hi:[0,0,0]
	s_setprio 0
	s_barrier
	ds_read_b128 v[46:49], v216 offset:0x4000
	ds_read_b128 v[50:53], v216 offset:0x4400
	ds_read_b128 v[54:57], v216 offset:0x4800
	ds_read_b128 v[58:61], v216 offset:0x4c00
	ds_read_b128 v[192:195], v216 offset:0x5000
	ds_read_b128 v[196:199], v216 offset:0x5400
	ds_read_b128 v[220:223], v216 offset:0x5800
	ds_read_b128 v[224:227], v216 offset:0x5c00
	s_mov_b32 m0, s71
	s_nop 0
	buffer_load_dwordx4 v215, s[8:11], s16 offen lds
	s_add_i32 s38, s16, 0x80000
	s_mov_b32 m0, s72
	s_nop 0
	buffer_load_dwordx4 v215, s[8:11], s38 offen lds
	s_add_i32 s38, s16, 0x8000
	s_mov_b32 m0, s73
	s_nop 0
	buffer_load_dwordx4 v215, s[8:11], s38 offen lds
	s_add_i32 s38, s16, 0x88000
	s_mov_b32 m0, s74
	s_nop 0
	buffer_load_dwordx4 v215, s[8:11], s38 offen lds
	s_mov_b32 m0, s70
	s_add_i32 s38, s65, 0x40000
	buffer_load_dwordx4 v214, s[12:15], s65 offen lds
	s_mov_b32 m0, s75
	s_nop 0
	buffer_load_dwordx4 v214, s[12:15], s38 offen lds
	s_waitcnt vmcnt(10)
	s_waitcnt lgkmcnt(0)
	s_barrier
	s_setprio 1
	v_mfma_scale_f32_16x16x128_f8f6f4 v[124:127], v[24:31], v[46:53], v[124:127], v213, v213 op_sel_hi:[0,0,0]
	v_mfma_scale_f32_16x16x128_f8f6f4 v[120:123], v[16:23], v[46:53], v[120:123], v213, v213 op_sel_hi:[0,0,0]
	v_mfma_scale_f32_16x16x128_f8f6f4 v[116:119], v[24:31], v[54:61], v[116:119], v213, v213 op_sel_hi:[0,0,0]
	v_mfma_scale_f32_16x16x128_f8f6f4 v[112:115], v[16:23], v[54:61], v[112:115], v213, v213 op_sel_hi:[0,0,0]
	v_mfma_scale_f32_16x16x128_f8f6f4 v[108:111], v[24:31], v[192:199], v[108:111], v213, v213 op_sel_hi:[0,0,0]
	v_mfma_scale_f32_16x16x128_f8f6f4 v[104:107], v[16:23], v[192:199], v[104:107], v213, v213 op_sel_hi:[0,0,0]
	v_mfma_scale_f32_16x16x128_f8f6f4 v[100:103], v[24:31], v[220:227], v[100:103], v213, v213 op_sel_hi:[0,0,0]
	v_mfma_scale_f32_16x16x128_f8f6f4 v[96:99], v[16:23], v[220:227], v[96:99], v213, v213 op_sel_hi:[0,0,0]
	s_setprio 0
	s_setprio 1
	v_mfma_scale_f32_16x16x128_f8f6f4 v[92:95], v[8:15], v[46:53], v[92:95], v213, v213 op_sel_hi:[0,0,0]
	v_mfma_scale_f32_16x16x128_f8f6f4 v[88:91], v[0:7], v[46:53], v[88:91], v213, v213 op_sel_hi:[0,0,0]
	v_mfma_scale_f32_16x16x128_f8f6f4 v[84:87], v[8:15], v[54:61], v[84:87], v213, v213 op_sel_hi:[0,0,0]
	v_mfma_scale_f32_16x16x128_f8f6f4 v[80:83], v[0:7], v[54:61], v[80:83], v213, v213 op_sel_hi:[0,0,0]
	v_mfma_scale_f32_16x16x128_f8f6f4 v[76:79], v[8:15], v[192:199], v[76:79], v213, v213 op_sel_hi:[0,0,0]
	v_mfma_scale_f32_16x16x128_f8f6f4 v[72:75], v[0:7], v[192:199], v[72:75], v213, v213 op_sel_hi:[0,0,0]
	v_mfma_scale_f32_16x16x128_f8f6f4 v[68:71], v[8:15], v[220:227], v[68:71], v213, v213 op_sel_hi:[0,0,0]
	v_mfma_scale_f32_16x16x128_f8f6f4 v[64:67], v[0:7], v[220:227], v[64:67], v213, v213 op_sel_hi:[0,0,0]
	s_setprio 0
	s_barrier
	ds_read_b128 v[16:19], v217 offset:0x8000
	ds_read_b128 v[20:23], v217 offset:0x8400
	ds_read_b128 v[24:27], v217 offset:0x8800
	ds_read_b128 v[28:31], v217 offset:0x8c00
	ds_read_b128 v[46:49], v216 offset:0x8000
	ds_read_b128 v[50:53], v216 offset:0x8400
	ds_read_b128 v[54:57], v216 offset:0x8800
	ds_read_b128 v[58:61], v216 offset:0x8c00
	ds_read_b128 v[192:195], v216 offset:0x9000
	ds_read_b128 v[196:199], v216 offset:0x9400
	ds_read_b128 v[220:223], v216 offset:0x9800
	ds_read_b128 v[224:227], v216 offset:0x9c00
	ds_read_b128 v[8:11], v217 offset:0xc000
	ds_read_b128 v[12:15], v217 offset:0xc400
	ds_read_b128 v[0:3], v217 offset:0xc800
	ds_read_b128 v[4:7], v217 offset:0xcc00
	s_mov_b32 m0, s76
	s_add_i32 s38, s65, 0x80000
	buffer_load_dwordx4 v214, s[12:15], s38 offen lds
	s_add_i32 s38, s65, 0xc0000
	s_mov_b32 m0, s77
	s_nop 0
	buffer_load_dwordx4 v214, s[12:15], s38 offen lds
	s_waitcnt vmcnt(10)
	s_waitcnt lgkmcnt(4)
	s_barrier
	s_setprio 1
	v_mfma_scale_f32_16x16x128_f8f6f4 v[188:191], v[16:23], v[46:53], v[188:191], v213, v213 op_sel_hi:[0,0,0]
	v_mfma_scale_f32_16x16x128_f8f6f4 v[184:187], v[24:31], v[46:53], v[184:187], v213, v213 op_sel_hi:[0,0,0]
	v_mfma_scale_f32_16x16x128_f8f6f4 v[180:183], v[16:23], v[54:61], v[180:183], v213, v213 op_sel_hi:[0,0,0]
	v_mfma_scale_f32_16x16x128_f8f6f4 v[176:179], v[24:31], v[54:61], v[176:179], v213, v213 op_sel_hi:[0,0,0]
	v_mfma_scale_f32_16x16x128_f8f6f4 v[172:175], v[16:23], v[192:199], v[172:175], v213, v213 op_sel_hi:[0,0,0]
	v_mfma_scale_f32_16x16x128_f8f6f4 v[168:171], v[24:31], v[192:199], v[168:171], v213, v213 op_sel_hi:[0,0,0]
	v_mfma_scale_f32_16x16x128_f8f6f4 v[164:167], v[16:23], v[220:227], v[164:167], v213, v213 op_sel_hi:[0,0,0]
	v_mfma_scale_f32_16x16x128_f8f6f4 v[160:163], v[24:31], v[220:227], v[160:163], v213, v213 op_sel_hi:[0,0,0]
	s_setprio 0
	s_setprio 1
	s_waitcnt lgkmcnt(2)
	v_mfma_scale_f32_16x16x128_f8f6f4 v[156:159], v[8:15], v[46:53], v[156:159], v213, v213 op_sel_hi:[0,0,0]
	s_waitcnt lgkmcnt(0)
	v_mfma_scale_f32_16x16x128_f8f6f4 v[152:155], v[0:7], v[46:53], v[152:155], v213, v213 op_sel_hi:[0,0,0]
	v_mfma_scale_f32_16x16x128_f8f6f4 v[148:151], v[8:15], v[54:61], v[148:151], v213, v213 op_sel_hi:[0,0,0]
	v_mfma_scale_f32_16x16x128_f8f6f4 v[144:147], v[0:7], v[54:61], v[144:147], v213, v213 op_sel_hi:[0,0,0]
	v_mfma_scale_f32_16x16x128_f8f6f4 v[140:143], v[8:15], v[192:199], v[140:143], v213, v213 op_sel_hi:[0,0,0]
	v_mfma_scale_f32_16x16x128_f8f6f4 v[136:139], v[0:7], v[192:199], v[136:139], v213, v213 op_sel_hi:[0,0,0]
	v_mfma_scale_f32_16x16x128_f8f6f4 v[132:135], v[8:15], v[220:227], v[132:135], v213, v213 op_sel_hi:[0,0,0]
	v_mfma_scale_f32_16x16x128_f8f6f4 v[128:131], v[0:7], v[220:227], v[128:131], v213, v213 op_sel_hi:[0,0,0]
	s_setprio 0
	s_barrier
	ds_read_b128 v[46:49], v216 offset:0xc000
	ds_read_b128 v[50:53], v216 offset:0xc400
	ds_read_b128 v[54:57], v216 offset:0xc800
	ds_read_b128 v[58:61], v216 offset:0xcc00
	ds_read_b128 v[192:195], v216 offset:0xd000
	ds_read_b128 v[196:199], v216 offset:0xd400
	ds_read_b128 v[220:223], v216 offset:0xd800
	ds_read_b128 v[224:227], v216 offset:0xdc00
	s_mov_b32 m0, s80
	s_nop 0
	buffer_load_dwordx4 v215, s[8:11], s17 offen lds
	s_add_i32 s17, s16, 0x80080
	s_mov_b32 m0, s81
	s_add_i32 s65, s65, 0x40080
	buffer_load_dwordx4 v215, s[8:11], s17 offen lds
	s_add_i32 s17, s16, 0x8080
	s_mov_b32 m0, s84
	s_add_i32 s16, s16, 0x88080
	buffer_load_dwordx4 v215, s[8:11], s17 offen lds
	s_mov_b32 m0, s85
	s_nop 0
	buffer_load_dwordx4 v215, s[8:11], s16 offen lds
	s_mov_b32 m0, s82
	s_nop 0
	buffer_load_dwordx4 v214, s[12:15], s3 offen lds
	s_mov_b32 m0, s83
	s_nop 0
	buffer_load_dwordx4 v214, s[12:15], s65 offen lds
	s_bitcmp0_b32 s64, 0
	s_mov_b32 s98, 0xffff
	s_cselect_b32 s98, 0xffff0000, s98
	s_waitcnt vmcnt(8)
	s_waitcnt lgkmcnt(0)
	s_barrier
	s_setprio 1
	v_mfma_scale_f32_16x16x128_f8f6f4 v[124:127], v[16:23], v[46:53], v[124:127], v213, v213 op_sel_hi:[0,0,0]
	v_mul_f32_e32 v32, 0x42800000, v32
	v_mul_f32_e32 v36, 0x42800000, v36
	v_mfma_scale_f32_16x16x128_f8f6f4 v[120:123], v[24:31], v[46:53], v[120:123], v213, v213 op_sel_hi:[0,0,0]
	v_mul_f32_e32 v33, 0x42800000, v33
	v_mul_f32_e32 v37, 0x42800000, v37
	v_mfma_scale_f32_16x16x128_f8f6f4 v[116:119], v[16:23], v[54:61], v[116:119], v213, v213 op_sel_hi:[0,0,0]
	v_mul_f32_e32 v34, 0x42800000, v34
	v_mul_f32_e32 v38, 0x42800000, v38
	v_mfma_scale_f32_16x16x128_f8f6f4 v[112:115], v[24:31], v[54:61], v[112:115], v213, v213 op_sel_hi:[0,0,0]
	v_mul_f32_e32 v35, 0x42800000, v35
	v_mul_f32_e32 v39, 0x42800000, v39
	v_mfma_scale_f32_16x16x128_f8f6f4 v[108:111], v[16:23], v[192:199], v[108:111], v213, v213 op_sel_hi:[0,0,0]
	v_cvt_pk_fp8_f32 v250, v32, v36
	v_mfma_scale_f32_16x16x128_f8f6f4 v[104:107], v[24:31], v[192:199], v[104:107], v213, v213 op_sel_hi:[0,0,0]
	v_cvt_pk_fp8_f32 v250, v32, v36 op_sel:[0,0,1]
	v_mfma_scale_f32_16x16x128_f8f6f4 v[100:103], v[16:23], v[220:227], v[100:103], v213, v213 op_sel_hi:[0,0,0]
	v_cvt_pk_fp8_f32 v251, v33, v37
	v_mfma_scale_f32_16x16x128_f8f6f4 v[96:99], v[24:31], v[220:227], v[96:99], v213, v213 op_sel_hi:[0,0,0]
	v_cvt_pk_fp8_f32 v251, v33, v37 op_sel:[0,0,1]
	s_setprio 0
	s_setprio 1
	v_mfma_scale_f32_16x16x128_f8f6f4 v[92:95], v[8:15], v[46:53], v[92:95], v213, v213 op_sel_hi:[0,0,0]
	v_cvt_pk_fp8_f32 v252, v34, v38
	v_mfma_scale_f32_16x16x128_f8f6f4 v[88:91], v[0:7], v[46:53], v[88:91], v213, v213 op_sel_hi:[0,0,0]
	v_cvt_pk_fp8_f32 v252, v34, v38 op_sel:[0,0,1]
	v_mfma_scale_f32_16x16x128_f8f6f4 v[84:87], v[8:15], v[54:61], v[84:87], v213, v213 op_sel_hi:[0,0,0]
	v_cvt_pk_fp8_f32 v253, v35, v39
	v_mfma_scale_f32_16x16x128_f8f6f4 v[80:83], v[0:7], v[54:61], v[80:83], v213, v213 op_sel_hi:[0,0,0]
	v_cvt_pk_fp8_f32 v253, v35, v39 op_sel:[0,0,1]
	v_mfma_scale_f32_16x16x128_f8f6f4 v[76:79], v[8:15], v[192:199], v[76:79], v213, v213 op_sel_hi:[0,0,0]
	v_bfi_b32 v40, s98, v250, v40
	v_mfma_scale_f32_16x16x128_f8f6f4 v[72:75], v[0:7], v[192:199], v[72:75], v213, v213 op_sel_hi:[0,0,0]
	v_bfi_b32 v41, s98, v251, v41
	v_mfma_scale_f32_16x16x128_f8f6f4 v[68:71], v[8:15], v[220:227], v[68:71], v213, v213 op_sel_hi:[0,0,0]
	v_bfi_b32 v42, s98, v252, v42
	v_mfma_scale_f32_16x16x128_f8f6f4 v[64:67], v[0:7], v[220:227], v[64:67], v213, v213 op_sel_hi:[0,0,0]
	v_bfi_b32 v43, s98, v253, v43
	s_setprio 0
	s_barrier
	s_bitcmp0_b32 s64, 0
	s_mov_b64 s[64:65], -1
	s_cbranch_scc0 .LBB0_924
	s_andn2_b64 vcc, exec, s[4:5]
	s_cbranch_vccnz .LBB0_924
	s_lshl_b64 s[4:5], s[62:63], 12
	v_mov_b32_e32 v0, s67
	v_or3_b32 v1, s5, 0, 0
	v_or3_b32 v0, s4, v0, v44
	v_lshlrev_b64 v[0:1], 9, v[0:1]
	v_lshl_add_u64 v[0:1], s[6:7], 0, v[0:1]
	s_lshl_b32 s36, s36, 7
	v_lshl_add_u64 v[0:1], v[0:1], 0, s[36:37]
	v_lshl_add_u64 v[0:1], v[0:1], 0, v[200:201]
	global_store_dword v[0:1], v40, off
	global_store_dword v[0:1], v41, off offset:512
	global_store_dword v[0:1], v42, off offset:1024
	global_store_dword v[0:1], v43, off offset:1536
	s_branch .LBB0_924
